# v5 plus MoE routing: next token row prefetched during the current token's reduction
# speedup vs baseline: 1.0019x; 1.0019x over previous
.LBB0_1203:
	s_ashr_i32 s9, s19, 6
	s_add_i32 s7, s9, s46
	s_cmp_ge_i32 s7, s6
	s_cbranch_scc1 .LBB0_1212
	s_lshl_b32 s8, s7, 1
	s_ashr_i32 s21, s9, 31
	s_ashr_i32 s24, s46, 31
	s_add_u32 s20, s9, s46
	s_addc_u32 s21, s21, s24
	s_mul_i32 s26, s44, 0x6410
	s_lshl_b64 s[24:25], s[20:21], 2
	s_mul_hi_i32 s19, s44, 0x6410
	s_add_u32 s9, s26, s24
	s_addc_u32 s19, s19, s25
	s_add_u32 s9, s4, s9
	s_addc_u32 s19, s5, s19
	s_add_u32 s64, s9, 0x18422000
	s_addc_u32 s65, s19, 0
	s_lshl_b64 s[20:21], s[20:21], 11
	v_and_b32_e32 v1, 63, v0
	s_add_u32 s20, s4, s20
	v_lshlrev_b32_e32 v2, 3, v1
	v_mov_b32_e32 v3, v48
	s_addc_u32 s21, s5, s21
	s_waitcnt vmcnt(0)
	v_lshlrev_b32_e32 v4, 7, v1
	v_lshl_add_u64 v[2:3], s[20:21], 0, v[2:3]
	s_mov_b64 s[20:21], 0x18422400
	v_cmp_eq_u32_e64 s[42:43], 0, v1
	v_lshl_add_u64 v[2:3], v[2:3], 0, s[20:21]
	v_add_u32_e32 v1, 0, v4
	global_load_dwordx2 v[50:51], v[2:3], off offset:-1024
	global_load_dwordx2 v[52:53], v[2:3], off offset:-512
	global_load_dwordx2 v[54:55], v[2:3], off
	global_load_dwordx2 v[56:57], v[2:3], off offset:512
	s_branch .LBB0_1206

.LBB0_1206:
	s_waitcnt vmcnt(0)
	v_mov_b32_e32 v4, v50
	v_mov_b32_e32 v5, v51
	v_mov_b32_e32 v26, v56
	v_mov_b32_e32 v27, v57
	v_and_b32_e32 v15, 0xffff0000, v5
	v_lshlrev_b32_e32 v16, 16, v4
	v_and_b32_e32 v17, 0xffff0000, v4
	v_lshlrev_b32_e32 v14, 16, v5
	v_mul_f32_e32 v4, v15, v15
	v_pk_fma_f32 v[22:23], v[14:15], v[14:15], v[4:5] op_sel_hi:[1,1,0]
	v_mov_b32_e32 v4, v52
	v_mov_b32_e32 v5, v53
	v_and_b32_e32 v21, 0xffff0000, v26
	v_lshlrev_b32_e32 v20, 16, v27
	v_and_b32_e32 v19, 0xffff0000, v27
	v_mov_b32_e32 v28, v22
	v_mul_f32_e32 v30, v21, v21
	v_mul_f32_e32 v31, v20, v20
	v_mul_f32_e32 v32, v19, v19
	v_and_b32_e32 v11, 0xffff0000, v5
	v_and_b32_e32 v10, 0xffff0000, v4
	v_lshlrev_b32_e32 v13, 16, v5
	v_lshlrev_b32_e32 v12, 16, v4
	v_pk_mul_f32 v[4:5], v[10:11], v[10:11]
	s_nop 0
	v_pk_fma_f32 v[24:25], v[12:13], v[12:13], v[4:5]
	v_mov_b32_e32 v4, v54
	v_mov_b32_e32 v5, v55
	s_add_i32 s32, s7, 8
	s_cmp_lt_i32 s32, s6
	s_cbranch_scc0 .Lmy_rt_np
	v_add_co_u32_e32 v58, vcc, 0x4000, v2
	s_nop 1
	v_addc_co_u32_e32 v59, vcc, 0, v3, vcc
	global_load_dwordx2 v[50:51], v[58:59], off offset:-1024
	global_load_dwordx2 v[52:53], v[58:59], off offset:-512
	global_load_dwordx2 v[54:55], v[58:59], off
	global_load_dwordx2 v[56:57], v[58:59], off offset:512
.Lmy_rt_np:
	v_pk_add_f32 v[24:25], v[24:25], v[24:25] op_sel:[0,1] op_sel_hi:[1,0]
	v_lshlrev_b32_e32 v8, 16, v4
	v_and_b32_e32 v9, 0xffff0000, v4
	v_lshlrev_b32_e32 v6, 16, v5
	v_and_b32_e32 v7, 0xffff0000, v5
	v_lshlrev_b32_e32 v5, 16, v26
	v_mul_f32_e32 v4, v17, v17
	v_pk_fma_f32 v[26:27], v[16:17], v[16:17], v[4:5] op_sel_hi:[1,1,0]
	v_mov_b32_e32 v29, v5
	v_mov_b32_e32 v4, v26
	v_pk_add_f32 v[22:23], v[26:27], v[22:23]
	v_pk_mul_f32 v[26:27], v[4:5], v[28:29]
	v_mov_b32_e32 v25, v30
	v_mov_b32_e32 v23, v27
	v_mul_f32_e32 v4, v9, v9
	v_pk_add_f32 v[22:23], v[22:23], v[24:25]
	v_pk_fma_f32 v[24:25], v[8:9], v[8:9], v[4:5] op_sel_hi:[1,1,0]
	v_mul_f32_e32 v4, v7, v7
	v_pk_fma_f32 v[26:27], v[6:7], v[6:7], v[4:5] op_sel_hi:[1,1,0]
	v_mov_b32_e32 v25, v31
	v_mov_b32_e32 v27, v32
	v_pk_add_f32 v[24:25], v[24:25], v[26:27]
	s_nop 0
	v_pk_add_f32 v[22:23], v[22:23], v[24:25]
	s_nop 0
	v_add_f32_e32 v4, v22, v23
	s_nop 1
	v_add_f32_dpp v4, v4, v4 quad_perm:[1,0,3,2] row_mask:0xf bank_mask:0xf bound_ctrl:1
	s_nop 1
	v_add_f32_dpp v4, v4, v4 quad_perm:[2,3,0,1] row_mask:0xf bank_mask:0xf bound_ctrl:1
	s_nop 1
	v_add_f32_dpp v4, v4, v4 row_half_mirror row_mask:0xf bank_mask:0xf bound_ctrl:1
	s_nop 1
	v_add_f32_dpp v4, v4, v4 row_mirror row_mask:0xf bank_mask:0xf bound_ctrl:1
	s_nop 0
	v_readlane_b32 s9, v4, 16
	v_readlane_b32 s19, v4, 48
	v_readlane_b32 s20, v4, 0
	v_readlane_b32 s21, v4, 32
	v_mov_b32_e32 v22, s9
	v_mov_b32_e32 v23, s19
	v_pk_add_f32 v[22:23], s[20:21], v[22:23]
	s_nop 0
	v_add_f32_e32 v4, v22, v23
	v_fmamk_f32 v4, v4, 0x3a800000, v237
	v_cmp_gt_f32_e32 vcc, s13, v4
	v_mul_f32_e32 v22, 0x4b800000, v4
	s_nop 0
	v_cndmask_b32_e32 v4, v4, v22, vcc
	v_rsq_f32_e32 v4, v4
	s_nop 0
	v_mul_f32_e32 v22, 0x45800000, v4
	v_cndmask_b32_e32 v4, v4, v22, vcc
	ds_read_b128 v[22:25], v1
	ds_read_b128 v[30:33], v1 offset:16
	ds_read_b128 v[34:37], v1 offset:32
	ds_read_b128 v[38:41], v1 offset:48
	v_mul_f32_e32 v16, v4, v16
	s_waitcnt lgkmcnt(3)
	v_fma_f32 v28, v22, v16, 0
	v_fma_f32 v27, v23, v16, 0
	v_fma_f32 v26, v24, v16, 0
	v_fma_f32 v25, v25, v16, 0
	v_mul_f32_e32 v17, v4, v17
	s_waitcnt lgkmcnt(2)
	v_fma_f32 v24, v30, v16, 0
	v_fma_f32 v23, v31, v16, 0
	v_fma_f32 v22, v32, v16, 0
	v_fma_f32 v16, v33, v16, 0
	s_waitcnt lgkmcnt(1)
	v_fmac_f32_e32 v28, v34, v17
	v_fmac_f32_e32 v27, v35, v17
	v_fmac_f32_e32 v26, v36, v17
	v_fmac_f32_e32 v25, v37, v17
	ds_read_b128 v[30:33], v1 offset:64
	ds_read_b128 v[34:37], v1 offset:80
	s_waitcnt lgkmcnt(2)
	v_fmac_f32_e32 v24, v38, v17
	v_fmac_f32_e32 v23, v39, v17
	v_fmac_f32_e32 v22, v40, v17
	v_fmac_f32_e32 v16, v41, v17
	v_mul_f32_e32 v14, v4, v14
	s_waitcnt lgkmcnt(1)
	v_fmac_f32_e32 v28, v30, v14
	v_fmac_f32_e32 v27, v31, v14
	v_fmac_f32_e32 v26, v32, v14
	v_fmac_f32_e32 v25, v33, v14
	s_waitcnt lgkmcnt(0)
	v_fmac_f32_e32 v24, v34, v14
	v_fmac_f32_e32 v23, v35, v14
	v_fmac_f32_e32 v22, v36, v14
	v_fmac_f32_e32 v16, v37, v14
	ds_read_b128 v[30:33], v1 offset:96
	ds_read_b128 v[34:37], v1 offset:112
	v_mul_f32_e32 v14, v4, v15
	v_mul_f32_e32 v12, v4, v12
	v_mul_f32_e32 v10, v4, v10
	s_waitcnt lgkmcnt(1)
	v_fmac_f32_e32 v28, v30, v14
	v_fmac_f32_e32 v27, v31, v14
	v_fmac_f32_e32 v26, v32, v14
	v_fmac_f32_e32 v25, v33, v14
	s_waitcnt lgkmcnt(0)
	v_fmac_f32_e32 v24, v34, v14
	v_fmac_f32_e32 v23, v35, v14
	v_fmac_f32_e32 v22, v36, v14
	v_fmac_f32_e32 v16, v37, v14
	ds_read_b128 v[30:33], v1 offset:8192
	ds_read_b128 v[34:37], v1 offset:8208
	v_mul_f32_e32 v8, v4, v8
	v_mul_f32_e32 v17, v4, v9
	v_mul_f32_e32 v6, v4, v6
	s_waitcnt lgkmcnt(1)
	v_fmac_f32_e32 v28, v30, v12
	v_fmac_f32_e32 v27, v31, v12
	v_fmac_f32_e32 v26, v32, v12
	v_fmac_f32_e32 v25, v33, v12
	s_waitcnt lgkmcnt(0)
	v_fmac_f32_e32 v24, v12, v34
	v_fmac_f32_e32 v23, v12, v35
	v_fmac_f32_e32 v22, v12, v36
	v_fmac_f32_e32 v16, v12, v37
	ds_read_b128 v[30:33], v1 offset:8224
	ds_read_b128 v[34:37], v1 offset:8240
	v_mul_f32_e32 v5, v4, v5
	s_waitcnt lgkmcnt(1)
	v_fmac_f32_e32 v28, v10, v30
	v_fmac_f32_e32 v27, v10, v31
	v_fmac_f32_e32 v26, v10, v32
	v_fmac_f32_e32 v25, v10, v33
	s_waitcnt lgkmcnt(0)
	v_fmac_f32_e32 v24, v10, v34
	v_fmac_f32_e32 v23, v10, v35
	v_fmac_f32_e32 v22, v10, v36
	v_fmac_f32_e32 v16, v10, v37
	v_mul_f32_e32 v10, v4, v13
	ds_read_b128 v[12:15], v1 offset:8256
	ds_read_b128 v[30:33], v1 offset:8272
	s_waitcnt lgkmcnt(1)
	v_fmac_f32_e32 v28, v10, v12
	v_fmac_f32_e32 v27, v10, v13
	v_fmac_f32_e32 v26, v10, v14
	v_fmac_f32_e32 v25, v10, v15
	s_waitcnt lgkmcnt(0)
	v_fmac_f32_e32 v24, v10, v30
	v_fmac_f32_e32 v23, v10, v31
	v_fmac_f32_e32 v22, v10, v32
	v_fmac_f32_e32 v16, v10, v33
	v_mul_f32_e32 v14, v4, v11
	ds_read_b128 v[10:13], v1 offset:8288
	ds_read_b128 v[30:33], v1 offset:8304
	s_waitcnt lgkmcnt(1)
	v_fmac_f32_e32 v28, v14, v10
	v_fmac_f32_e32 v27, v14, v11
	v_fmac_f32_e32 v26, v14, v12
	v_fmac_f32_e32 v25, v14, v13
	s_waitcnt lgkmcnt(0)
	v_fmac_f32_e32 v24, v14, v30
	v_fmac_f32_e32 v23, v14, v31
	v_fmac_f32_e32 v22, v14, v32
	v_fmac_f32_e32 v16, v14, v33
	ds_read_b128 v[10:13], v1 offset:16384
	ds_read_b128 v[30:33], v1 offset:16400
	s_waitcnt lgkmcnt(1)
	v_fmac_f32_e32 v28, v8, v10
	v_fmac_f32_e32 v27, v8, v11
	v_fmac_f32_e32 v26, v8, v12
	v_fmac_f32_e32 v25, v8, v13
	s_waitcnt lgkmcnt(0)
	v_fmac_f32_e32 v24, v8, v30
	v_fmac_f32_e32 v23, v8, v31
	v_fmac_f32_e32 v22, v8, v32
	v_fmac_f32_e32 v16, v8, v33
	ds_read_b128 v[8:11], v1 offset:16416
	ds_read_b128 v[12:15], v1 offset:16432
	s_waitcnt lgkmcnt(1)
	v_fmac_f32_e32 v28, v17, v8
	v_fmac_f32_e32 v27, v17, v9
	v_fmac_f32_e32 v26, v17, v10
	v_fmac_f32_e32 v25, v17, v11
	s_waitcnt lgkmcnt(0)
	v_fmac_f32_e32 v24, v17, v12
	v_fmac_f32_e32 v23, v17, v13
	v_fmac_f32_e32 v22, v17, v14
	v_fmac_f32_e32 v16, v17, v15
	ds_read_b128 v[8:11], v1 offset:16448
	ds_read_b128 v[12:15], v1 offset:16464
	s_waitcnt lgkmcnt(1)
	v_fmac_f32_e32 v28, v6, v8
	v_fmac_f32_e32 v27, v6, v9
	v_fmac_f32_e32 v26, v6, v10
	v_fmac_f32_e32 v25, v6, v11
	s_waitcnt lgkmcnt(0)
	v_fmac_f32_e32 v24, v6, v12
	v_fmac_f32_e32 v23, v6, v13
	v_fmac_f32_e32 v22, v6, v14
	v_fmac_f32_e32 v16, v6, v15
	v_mul_f32_e32 v14, v4, v7
	ds_read_b128 v[6:9], v1 offset:16480
	ds_read_b128 v[10:13], v1 offset:16496
	s_waitcnt lgkmcnt(1)
	v_fmac_f32_e32 v28, v14, v6
	v_fmac_f32_e32 v27, v14, v7
	v_fmac_f32_e32 v26, v14, v8
	v_fmac_f32_e32 v25, v14, v9
	s_waitcnt lgkmcnt(0)
	v_fmac_f32_e32 v24, v14, v10
	v_fmac_f32_e32 v23, v14, v11
	v_fmac_f32_e32 v22, v14, v12
	v_fmac_f32_e32 v16, v14, v13
	ds_read_b128 v[6:9], v1 offset:24576
	ds_read_b128 v[10:13], v1 offset:24592
	s_waitcnt lgkmcnt(1)
	v_fmac_f32_e32 v28, v5, v6
	v_fmac_f32_e32 v27, v5, v7
	v_fmac_f32_e32 v26, v5, v8
	v_fmac_f32_e32 v25, v5, v9
	s_waitcnt lgkmcnt(0)
	v_fmac_f32_e32 v24, v5, v10
	v_fmac_f32_e32 v23, v5, v11
	v_fmac_f32_e32 v22, v5, v12
	v_fmac_f32_e32 v16, v5, v13
	ds_read_b128 v[6:9], v1 offset:24608
	ds_read_b128 v[10:13], v1 offset:24624
	v_mul_f32_e32 v5, v4, v21
	s_waitcnt lgkmcnt(1)
	v_fmac_f32_e32 v28, v5, v6
	v_fmac_f32_e32 v27, v5, v7
	v_fmac_f32_e32 v26, v5, v8
	v_fmac_f32_e32 v25, v5, v9
	s_waitcnt lgkmcnt(0)
	v_fmac_f32_e32 v24, v5, v10
	v_fmac_f32_e32 v23, v5, v11
	v_fmac_f32_e32 v22, v5, v12
	v_fmac_f32_e32 v16, v5, v13
	ds_read_b128 v[6:9], v1 offset:24640
	ds_read_b128 v[10:13], v1 offset:24656
	v_mul_f32_e32 v5, v4, v20
	s_waitcnt lgkmcnt(1)
	v_fmac_f32_e32 v28, v5, v6
	v_fmac_f32_e32 v27, v5, v7
	v_fmac_f32_e32 v26, v5, v8
	v_fmac_f32_e32 v25, v5, v9
	s_waitcnt lgkmcnt(0)
	v_fmac_f32_e32 v24, v5, v10
	v_fmac_f32_e32 v23, v5, v11
	v_fmac_f32_e32 v22, v5, v12
	v_fmac_f32_e32 v16, v5, v13
	ds_read_b128 v[6:9], v1 offset:24672
	ds_read_b128 v[10:13], v1 offset:24688
	v_mul_f32_e32 v5, v4, v19
	s_waitcnt lgkmcnt(1)
	v_fmac_f32_e32 v28, v5, v6
	v_fmac_f32_e32 v27, v5, v7
	v_fmac_f32_e32 v26, v5, v8
	v_fmac_f32_e32 v25, v5, v9
	s_waitcnt lgkmcnt(0)
	v_fmac_f32_e32 v24, v5, v10
	v_fmac_f32_e32 v23, v5, v11
	v_fmac_f32_e32 v22, v5, v12
	v_fmac_f32_e32 v16, v5, v13
	v_add_f32_dpp v5, v28, v28 quad_perm:[1,0,3,2] row_mask:0xf bank_mask:0xf bound_ctrl:1
	s_nop 1
	v_add_f32_dpp v5, v5, v5 quad_perm:[2,3,0,1] row_mask:0xf bank_mask:0xf bound_ctrl:1
	s_nop 1
	v_add_f32_dpp v5, v5, v5 row_half_mirror row_mask:0xf bank_mask:0xf bound_ctrl:1
	s_nop 1
	v_add_f32_dpp v5, v5, v5 row_mirror row_mask:0xf bank_mask:0xf bound_ctrl:1
	s_nop 0
	v_readlane_b32 s44, v5, 0
	v_readlane_b32 s9, v5, 16
	v_readlane_b32 s45, v5, 32
	v_readlane_b32 s19, v5, 48
	v_add_f32_dpp v5, v27, v27 quad_perm:[1,0,3,2] row_mask:0xf bank_mask:0xf bound_ctrl:1
	s_nop 1
	v_add_f32_dpp v5, v5, v5 quad_perm:[2,3,0,1] row_mask:0xf bank_mask:0xf bound_ctrl:1
	s_nop 1
	v_add_f32_dpp v5, v5, v5 row_half_mirror row_mask:0xf bank_mask:0xf bound_ctrl:1
	s_nop 1
	v_add_f32_dpp v5, v5, v5 row_mirror row_mask:0xf bank_mask:0xf bound_ctrl:1
	s_nop 0
	v_readlane_b32 s46, v5, 0
	v_readlane_b32 s20, v5, 16
	v_readlane_b32 s47, v5, 32
	v_readlane_b32 s21, v5, 48
	v_add_f32_dpp v5, v26, v26 quad_perm:[1,0,3,2] row_mask:0xf bank_mask:0xf bound_ctrl:1
	s_nop 1
	v_add_f32_dpp v5, v5, v5 quad_perm:[2,3,0,1] row_mask:0xf bank_mask:0xf bound_ctrl:1
	s_nop 1
	v_add_f32_dpp v5, v5, v5 row_half_mirror row_mask:0xf bank_mask:0xf bound_ctrl:1
	s_nop 1
	v_add_f32_dpp v5, v5, v5 row_mirror row_mask:0xf bank_mask:0xf bound_ctrl:1
	s_nop 0
	v_readlane_b32 s48, v5, 0
	v_readlane_b32 s24, v5, 16
	v_readlane_b32 s49, v5, 32
	v_readlane_b32 s25, v5, 48
	v_add_f32_dpp v5, v25, v25 quad_perm:[1,0,3,2] row_mask:0xf bank_mask:0xf bound_ctrl:1
	s_nop 1
	v_add_f32_dpp v5, v5, v5 quad_perm:[2,3,0,1] row_mask:0xf bank_mask:0xf bound_ctrl:1
	s_nop 1
	v_add_f32_dpp v5, v5, v5 row_half_mirror row_mask:0xf bank_mask:0xf bound_ctrl:1
	s_nop 1
	v_add_f32_dpp v5, v5, v5 row_mirror row_mask:0xf bank_mask:0xf bound_ctrl:1
	s_nop 0
	v_readlane_b32 s50, v5, 0
	v_readlane_b32 s26, v5, 16
	v_readlane_b32 s51, v5, 32
	v_readlane_b32 s28, v5, 48
	v_add_f32_dpp v5, v24, v24 quad_perm:[1,0,3,2] row_mask:0xf bank_mask:0xf bound_ctrl:1
	s_nop 1
	v_add_f32_dpp v5, v5, v5 quad_perm:[2,3,0,1] row_mask:0xf bank_mask:0xf bound_ctrl:1
	s_nop 1
	v_add_f32_dpp v5, v5, v5 row_half_mirror row_mask:0xf bank_mask:0xf bound_ctrl:1
	s_nop 1
	v_add_f32_dpp v5, v5, v5 row_mirror row_mask:0xf bank_mask:0xf bound_ctrl:1
	s_nop 0
	v_readlane_b32 s52, v5, 0
	v_readlane_b32 s29, v5, 16
	v_readlane_b32 s53, v5, 32
	v_readlane_b32 s30, v5, 48
	v_add_f32_dpp v5, v23, v23 quad_perm:[1,0,3,2] row_mask:0xf bank_mask:0xf bound_ctrl:1
	s_nop 1
	v_add_f32_dpp v5, v5, v5 quad_perm:[2,3,0,1] row_mask:0xf bank_mask:0xf bound_ctrl:1
	s_nop 1
	v_add_f32_dpp v5, v5, v5 row_half_mirror row_mask:0xf bank_mask:0xf bound_ctrl:1
	s_nop 1
	v_add_f32_dpp v5, v5, v5 row_mirror row_mask:0xf bank_mask:0xf bound_ctrl:1
	s_nop 0
	v_readlane_b32 s54, v5, 0
	v_readlane_b32 s38, v5, 16
	v_readlane_b32 s55, v5, 32
	v_readlane_b32 s39, v5, 48
	v_add_f32_dpp v5, v22, v22 quad_perm:[1,0,3,2] row_mask:0xf bank_mask:0xf bound_ctrl:1
	s_nop 1
	v_add_f32_dpp v5, v5, v5 quad_perm:[2,3,0,1] row_mask:0xf bank_mask:0xf bound_ctrl:1
	s_nop 1
	v_add_f32_dpp v5, v5, v5 row_half_mirror row_mask:0xf bank_mask:0xf bound_ctrl:1
	s_nop 1
	v_add_f32_dpp v5, v5, v5 row_mirror row_mask:0xf bank_mask:0xf bound_ctrl:1
	s_nop 0
	v_readlane_b32 s56, v5, 0
	v_readlane_b32 s60, v5, 16
	v_readlane_b32 s57, v5, 32
	v_readlane_b32 s61, v5, 48
	v_add_f32_dpp v5, v16, v16 quad_perm:[1,0,3,2] row_mask:0xf bank_mask:0xf bound_ctrl:1
	s_nop 1
	v_add_f32_dpp v5, v5, v5 quad_perm:[2,3,0,1] row_mask:0xf bank_mask:0xf bound_ctrl:1
	s_nop 1
	v_add_f32_dpp v5, v5, v5 row_half_mirror row_mask:0xf bank_mask:0xf bound_ctrl:1
	s_nop 1
	v_add_f32_dpp v5, v5, v5 row_mirror row_mask:0xf bank_mask:0xf bound_ctrl:1
	s_nop 0
	v_readlane_b32 s58, v5, 0
	v_readlane_b32 s62, v5, 16
	v_readlane_b32 s59, v5, 32
	v_readlane_b32 s63, v5, 48
	s_and_saveexec_b64 s[66:67], s[42:43]
	s_cbranch_execz .LBB0_1205
	v_mov_b32_e32 v6, s62
	v_mov_b32_e32 v7, s63
	v_pk_add_f32 v[6:7], s[58:59], v[6:7]
	v_mov_b32_e32 v8, s9
	v_add_f32_e32 v5, v6, v7
	v_mov_b32_e32 v6, s60
	v_mov_b32_e32 v7, s61
	v_pk_add_f32 v[6:7], s[56:57], v[6:7]
	v_mov_b32_e32 v9, s19
	v_add_f32_e32 v12, v6, v7
	v_mov_b32_e32 v6, s38
	v_mov_b32_e32 v7, s39
	v_pk_add_f32 v[6:7], s[54:55], v[6:7]
	v_pk_add_f32 v[8:9], s[44:45], v[8:9]
	v_add_f32_e32 v13, v6, v7
	v_mov_b32_e32 v6, s29
	v_mov_b32_e32 v7, s30
	v_pk_add_f32 v[6:7], s[52:53], v[6:7]
	v_mov_b32_e32 v11, v8
	v_add_f32_e32 v14, v6, v7
	v_mov_b32_e32 v6, s26
	v_mov_b32_e32 v7, s28
	v_pk_add_f32 v[6:7], s[50:51], v[6:7]
	s_nop 0
	v_add_f32_e32 v15, v6, v7
	v_mov_b32_e32 v6, s24
	v_mov_b32_e32 v7, s25
	v_pk_add_f32 v[6:7], s[48:49], v[6:7]
	s_nop 0
	v_add_f32_e32 v16, v6, v7
	v_mov_b32_e32 v6, s20
	v_mov_b32_e32 v7, s21
	v_pk_add_f32 v[6:7], s[46:47], v[6:7]
	s_nop 0
	v_mov_b32_e32 v10, v6
	v_mov_b32_e32 v8, v7
	v_pk_add_f32 v[6:7], v[10:11], v[8:9]
	s_nop 0
	v_cmp_gt_f32_e32 vcc, v6, v7
	s_nop 1
	v_cndmask_b32_e32 v8, v7, v6, vcc
	v_cmp_gt_f32_e64 s[44:45], v16, v8
	v_cndmask_b32_e64 v9, 0, 1, vcc
	v_cmp_nlg_f32_e32 vcc, s82, v7
	v_cndmask_b32_e64 v8, v8, v16, s[44:45]
	v_cmp_gt_f32_e64 s[46:47], v15, v8
	v_readfirstlane_b32 s9, v9
	s_nop 0
	v_cndmask_b32_e64 v8, v8, v15, s[46:47]
	v_cmp_gt_f32_e64 s[48:49], v14, v8
	s_nop 1
	v_cndmask_b32_e64 v8, v8, v14, s[48:49]
	v_cmp_gt_f32_e64 s[50:51], v13, v8
	s_nop 1
	v_cndmask_b32_e64 v8, v8, v13, s[50:51]
	v_cmp_gt_f32_e64 s[52:53], v12, v8
	s_nop 1
	v_cndmask_b32_e64 v8, v8, v12, s[52:53]
	v_cmp_ngt_f32_e64 s[54:55], v5, v8
	s_and_b64 s[20:21], s[52:53], s[54:55]
	s_and_b64 s[24:25], s[44:45], exec
	s_cselect_b32 s9, 2, s9
	s_and_b64 s[24:25], s[46:47], exec
	s_cselect_b32 s9, 3, s9
	s_and_b64 s[24:25], s[48:49], exec
	s_cselect_b32 s9, 4, s9
	s_and_b64 s[24:25], s[50:51], exec
	s_cselect_b32 s9, 5, s9
	s_and_b64 s[24:25], s[52:53], exec
	s_cselect_b32 s9, 6, s9
	s_and_b64 s[24:25], s[54:55], exec
	s_cselect_b32 s19, s9, 7
	s_cmp_lg_u32 s19, 5
	s_cselect_b64 s[24:25], -1, 0
	s_cmp_lg_u32 s19, 4
	s_cselect_b64 s[28:29], -1, 0
	s_cmp_lg_u32 s19, 3
	s_cselect_b64 s[38:39], -1, 0
	s_cmp_lg_u32 s19, 2
	s_cselect_b64 s[48:49], -1, 0
	s_cmp_lg_u32 s19, 1
	s_cselect_b64 s[46:47], -1, 0
	s_cmp_eq_u32 s19, 0
	s_cselect_b64 s[44:45], -1, 0
	s_or_b64 vcc, s[44:45], vcc
	v_cndmask_b32_e32 v7, v7, v244, vcc
	v_cmp_gt_f32_e64 s[44:45], v6, v7
	s_and_b64 s[44:45], s[46:47], s[44:45]
	s_nop 0
	v_cndmask_b32_e64 v6, v7, v6, s[44:45]
	v_cmp_gt_f32_e64 s[46:47], v16, v6
	s_and_b64 s[46:47], s[48:49], s[46:47]
	v_cndmask_b32_e64 v7, 0, -1, vcc
	v_cndmask_b32_e64 v6, v6, v16, s[46:47]
	v_cmp_gt_f32_e64 s[48:49], v15, v6
	s_and_b64 s[48:49], s[38:39], s[48:49]
	v_readfirstlane_b32 s9, v7
	v_cndmask_b32_e64 v6, v6, v15, s[48:49]
	v_cmp_gt_f32_e64 s[50:51], v14, v6
	s_and_b64 s[50:51], s[28:29], s[50:51]
	s_nop 0
	v_cndmask_b32_e64 v6, v6, v14, s[50:51]
	v_cmp_gt_f32_e64 s[52:53], v13, v6
	s_and_b64 s[52:53], s[24:25], s[52:53]
	s_nop 0
	v_cndmask_b32_e64 v6, v6, v13, s[52:53]
	v_cmp_ngt_f32_e64 s[56:57], v12, v6
	s_or_b64 s[56:57], s[20:21], s[56:57]
	s_nop 0
	v_cndmask_b32_e64 v6, v12, v6, s[56:57]
	v_cmp_gt_f32_e64 s[58:59], v5, v6
	s_and_b64 s[58:59], s[54:55], s[58:59]
	s_and_b64 s[20:21], s[44:45], exec
	v_cndmask_b32_e64 v6, v6, v5, s[58:59]
	v_cndmask_b32_e64 v5, v5, v8, s[54:55]
	v_sub_f32_e32 v5, v6, v5
	v_mul_f32_e32 v5, 0x3fb8aa3b, v5
	v_exp_f32_e32 v5, v5
	s_cselect_b32 s9, 1, s9
	s_and_b64 s[20:21], s[46:47], exec
	s_cselect_b32 s9, 2, s9
	v_add_f32_e32 v5, 1.0, v5
	v_div_scale_f32 v6, s[24:25], v5, v5, 1.0
	v_rcp_f32_e32 v7, v6
	s_and_b64 s[20:21], s[48:49], exec
	s_cselect_b32 s9, 3, s9
	s_and_b64 s[20:21], s[50:51], exec
	s_cselect_b32 s9, 4, s9
	s_and_b64 s[20:21], s[52:53], exec
	v_fma_f32 v8, -v6, v7, 1.0
	s_cselect_b32 s9, 5, s9
	s_and_b64 s[20:21], s[56:57], exec
	v_fmac_f32_e32 v7, v8, v7
	v_div_scale_f32 v8, vcc, 1.0, v5, 1.0
	s_cselect_b32 s9, s9, 6
	s_and_b64 s[20:21], s[58:59], exec
	v_mul_f32_e32 v9, v8, v7
	s_cselect_b32 s20, 7, s9
	v_fma_f32 v10, -v6, v9, v8
	s_ashr_i32 s9, s8, 31
	v_fmac_f32_e32 v9, v10, v7
	s_lshl_b64 s[24:25], s[8:9], 2
	v_fma_f32 v6, -v6, v9, v8
	s_add_u32 s28, s1, s24
	v_div_fmas_f32 v6, v6, v7, v9
	s_addc_u32 s29, s12, s25
	v_div_fixup_f32 v6, v6, v5, 1.0
	s_add_u32 s24, s17, s24
	v_mov_b32_e32 v8, s19
	v_mov_b32_e32 v9, s20
	s_addc_u32 s25, s18, s25
	v_sub_f32_e32 v7, 1.0, v6
	s_mov_b64 s[44:45], exec
	global_store_dwordx2 v48, v[8:9], s[28:29]
	global_store_dwordx2 v48, v[6:7], s[24:25]
	global_store_dword v48, v4, s[64:65]
	v_mbcnt_lo_u32_b32 v4, s44, 0
	v_mbcnt_hi_u32_b32 v4, s45, v4
	v_cmp_eq_u32_e32 vcc, 0, v4
	s_and_saveexec_b64 s[46:47], vcc
	s_cbranch_execz .LBB0_1209
	s_lshl_b32 s9, s19, 2
	s_add_i32 s9, s9, 0
	s_add_i32 s9, s9, 0x23c40
	s_bcnt1_i32_b64 s19, s[44:45]
	v_mov_b32_e32 v4, s9
	v_mov_b32_e32 v5, s19
	ds_add_u32 v4, v5
